# speedup vs baseline: 1.0462x; 1.0039x over previous
.LBB1_8:
	s_lshl_b32 s12, s62, 9
	v_lshl_add_u64 v[6:7], s[12:13], 4, v[210:211]
	v_add_co_u32_e32 v34, vcc, s52, v6
	s_mov_b32 s12, s13
	s_nop 0
	v_addc_co_u32_e32 v35, vcc, 0, v7, vcc
	global_load_dwordx4 v[2:5], v[34:35], off offset:-4096
	v_add_co_u32_e32 v36, vcc, s49, v6
	s_xor_b64 s[50:51], s[14:15], -1
	s_nop 0
	v_addc_co_u32_e32 v37, vcc, 0, v7, vcc
	global_load_dwordx4 v[6:9], v[36:37], off offset:1024
	global_load_dwordx4 v[10:13], v[36:37], off offset:2048
	global_load_dwordx4 v[14:17], v[34:35], off
	s_mov_b32 s14, s13
	s_mov_b32 s15, s13
	s_mov_b32 s16, s13
	s_mov_b32 s17, s13
	s_mov_b32 s18, s13
	s_mov_b32 s19, s13
	s_mov_b32 s20, s13
	s_mov_b32 s21, s13
	s_mov_b32 s22, s13
	s_mov_b32 s23, s13
	s_mov_b32 s24, s13
	s_mov_b32 s25, s13
	s_mov_b32 s26, s13
	s_mov_b32 s27, s13
	s_waitcnt vmcnt(3) lgkmcnt(7)
	v_mfma_f32_32x32x16_f16 v[18:33], v[2:5], v[146:149], 0
	global_load_dwordx4 v[2:5], v[36:37], off offset:3072
	s_waitcnt vmcnt(3) lgkmcnt(6)
	v_mfma_f32_32x32x16_f16 v[18:33], v[6:9], v[150:153], v[18:33]
	global_load_dwordx4 v[6:9], v[34:35], off offset:1024
	s_waitcnt vmcnt(3) lgkmcnt(5)
	v_mfma_f32_32x32x16_f16 v[18:33], v[10:13], v[154:157], v[18:33]
	global_load_dwordx4 v[10:13], v[34:35], off offset:2048
	s_nop 0
	global_load_dwordx4 v[34:37], v[34:35], off offset:3072
	s_waitcnt vmcnt(3) lgkmcnt(4)
	v_mfma_f32_32x32x16_f16 v[18:33], v[2:5], v[158:161], v[18:33]
	s_waitcnt lgkmcnt(3)
	v_mfma_f32_32x32x16_f16 v[18:33], v[14:17], v[162:165], v[18:33]
	s_waitcnt vmcnt(2) lgkmcnt(2)
	v_mfma_f32_32x32x16_f16 v[18:33], v[6:9], v[166:169], v[18:33]
	s_waitcnt vmcnt(1) lgkmcnt(1)
	v_mfma_f32_32x32x16_f16 v[18:33], v[10:13], v[170:173], v[18:33]
	v_mov_b64_e32 v[2:3], s[12:13]
	v_mov_b64_e32 v[4:5], s[14:15]
	v_mov_b64_e32 v[6:7], s[16:17]
	v_mov_b64_e32 v[8:9], s[18:19]
	v_mov_b64_e32 v[10:11], s[20:21]
	v_mov_b64_e32 v[12:13], s[22:23]
	v_mov_b64_e32 v[14:15], s[24:25]
	s_waitcnt vmcnt(0) lgkmcnt(0)
	v_mfma_f32_32x32x16_f16 v[18:33], v[34:37], v[174:177], v[18:33]
	v_mov_b64_e32 v[16:17], s[26:27]
	s_mul_i32 s12, s62, 20
	s_lshl_b64 s[14:15], s[12:13], 2
	s_add_u32 s14, s10, s14
	s_addc_u32 s15, s11, s15
	s_load_dwordx16 s[16:31], s[14:15], 0x0
	s_load_dwordx4 s[40:43], s[14:15], 0x40
	s_mul_i32 s12, s62, 0x1b0000
	s_nop 3
	ds_bpermute_b32 v34, v225, v18
	ds_bpermute_b32 v35, v225, v19
	ds_bpermute_b32 v36, v225, v20
	ds_bpermute_b32 v37, v225, v21
	ds_bpermute_b32 v38, v225, v22
	ds_bpermute_b32 v39, v225, v23
	ds_bpermute_b32 v40, v225, v24
	ds_bpermute_b32 v41, v225, v25
	ds_bpermute_b32 v42, v225, v26
	ds_bpermute_b32 v43, v225, v27
	ds_bpermute_b32 v44, v225, v28
	ds_bpermute_b32 v45, v225, v29
	ds_bpermute_b32 v46, v225, v30
	ds_bpermute_b32 v47, v225, v31
	ds_bpermute_b32 v48, v225, v32
	ds_bpermute_b32 v49, v225, v33
	s_waitcnt lgkmcnt(0)
	v_cndmask_b32_e64 v50, v34, v18, s[0:1]
	v_cndmask_b32_e64 v19, v35, v19, s[0:1]
	v_cndmask_b32_e64 v20, v36, v20, s[0:1]
	v_cndmask_b32_e64 v21, v37, v21, s[0:1]
	v_cndmask_b32_e64 v18, v18, v34, s[0:1]
	v_cndmask_b32_e64 v34, v38, v22, s[0:1]
	v_cndmask_b32_e64 v23, v39, v23, s[0:1]
	v_cndmask_b32_e64 v24, v40, v24, s[0:1]
	v_cndmask_b32_e64 v25, v41, v25, s[0:1]
	v_cndmask_b32_e64 v22, v22, v38, s[0:1]
	v_add_f32_e32 v37, s16, v50
	v_add_f32_e32 v19, s17, v19
	v_add_f32_e32 v20, s18, v20
	v_add_f32_e32 v21, s19, v21
	v_add_f32_e32 v34, s21, v34
	v_add_f32_e32 v23, s22, v23
	v_add_f32_e32 v24, s23, v24
	v_add_f32_e32 v25, s24, v25
	v_cndmask_b32_e64 v35, v42, v26, s[0:1]
	v_cndmask_b32_e64 v27, v43, v27, s[0:1]
	v_cndmask_b32_e64 v28, v44, v28, s[0:1]
	v_cndmask_b32_e64 v29, v45, v29, s[0:1]
	v_add_f32_e32 v18, s20, v18
	v_add_f32_e32 v22, s25, v22
	v_max_f32_e32 v38, v37, v19
	v_max_f32_e32 v39, v20, v21
	v_max_f32_e32 v40, v34, v23
	v_max_f32_e32 v41, v24, v25
	v_cndmask_b32_e64 v26, v26, v42, s[0:1]
	v_cndmask_b32_e64 v36, v46, v30, s[0:1]
	v_cndmask_b32_e64 v31, v47, v31, s[0:1]
	v_cndmask_b32_e64 v32, v48, v32, s[0:1]
	v_add_f32_e32 v35, s26, v35
	v_add_f32_e32 v27, s27, v27
	v_add_f32_e32 v28, s28, v28
	v_add_f32_e32 v29, s29, v29
	v_max3_f32 v38, v38, v39, v18
	v_max3_f32 v39, v40, v41, v22
	v_cndmask_b32_e64 v33, v49, v33, s[0:1]
	v_add_f32_e32 v26, s30, v26
	v_add_f32_e32 v36, s31, v36
	v_add_f32_e32 v31, s40, v31
	v_add_f32_e32 v32, s41, v32
	v_max_f32_e32 v42, v35, v27
	v_max_f32_e32 v43, v28, v29
	v_sub_f32_e32 v34, v34, v39
	v_add_f32_e32 v33, s42, v33
	v_cndmask_b32_e64 v30, v30, v46, s[0:1]
	v_max3_f32 v40, v42, v43, v26
	v_sub_f32_e32 v37, v37, v38
	v_sub_f32_e32 v23, v23, v39
	v_mul_f32_e32 v34, 0x3fb8aa3b, v34
	v_add_f32_e32 v30, s43, v30
	v_max_f32_e32 v41, v36, v31
	v_max_f32_e32 v42, v32, v33
	v_sub_f32_e32 v19, v19, v38
	v_sub_f32_e32 v24, v24, v39
	v_sub_f32_e32 v35, v35, v40
	v_mul_f32_e32 v37, 0x3fb8aa3b, v37
	v_mul_f32_e32 v23, 0x3fb8aa3b, v23
	v_exp_f32_e32 v34, v34
	v_max3_f32 v41, v41, v42, v30
	v_sub_f32_e32 v20, v20, v38
	v_sub_f32_e32 v25, v25, v39
	v_sub_f32_e32 v27, v27, v40
	v_mul_f32_e32 v19, 0x3fb8aa3b, v19
	v_mul_f32_e32 v24, 0x3fb8aa3b, v24
	v_mul_f32_e32 v35, 0x3fb8aa3b, v35
	v_exp_f32_e32 v37, v37
	v_exp_f32_e32 v23, v23
	v_sub_f32_e32 v36, v36, v41
	v_sub_f32_e32 v21, v21, v38
	v_sub_f32_e32 v22, v22, v39
	v_sub_f32_e32 v28, v28, v40
	v_mul_f32_e32 v20, 0x3fb8aa3b, v20
	v_mul_f32_e32 v25, 0x3fb8aa3b, v25
	v_mul_f32_e32 v27, 0x3fb8aa3b, v27
	v_exp_f32_e32 v19, v19
	v_exp_f32_e32 v24, v24
	v_exp_f32_e32 v35, v35
	v_mul_f32_e32 v36, 0x3fb8aa3b, v36
	v_sub_f32_e32 v31, v31, v41
	v_sub_f32_e32 v18, v18, v38
	v_sub_f32_e32 v29, v29, v40
	v_mul_f32_e32 v21, 0x3fb8aa3b, v21
	v_mul_f32_e32 v22, 0x3fb8aa3b, v22
	v_mul_f32_e32 v28, 0x3fb8aa3b, v28
	v_exp_f32_e32 v20, v20
	v_exp_f32_e32 v25, v25
	v_exp_f32_e32 v27, v27
	v_exp_f32_e32 v36, v36
	v_mul_f32_e32 v31, 0x3fb8aa3b, v31
	v_sub_f32_e32 v32, v32, v41
	v_sub_f32_e32 v26, v26, v40
	v_mul_f32_e32 v18, 0x3fb8aa3b, v18
	v_mul_f32_e32 v29, 0x3fb8aa3b, v29
	v_exp_f32_e32 v21, v21
	v_exp_f32_e32 v22, v22
	v_exp_f32_e32 v28, v28
	v_add_f32_e32 v39, 0, v34
	v_exp_f32_e32 v31, v31
	v_mul_f32_e32 v32, 0x3fb8aa3b, v32
	v_sub_f32_e32 v33, v33, v41
	v_mul_f32_e32 v26, 0x3fb8aa3b, v26
	v_exp_f32_e32 v18, v18
	v_exp_f32_e32 v29, v29
	v_add_f32_e32 v38, 0, v37
	v_add_f32_e32 v39, v23, v39
	v_exp_f32_e32 v32, v32
	v_mul_f32_e32 v33, 0x3fb8aa3b, v33
	v_sub_f32_e32 v30, v30, v41
	v_exp_f32_e32 v26, v26
	v_add_f32_e32 v40, 0, v35
	v_add_f32_e32 v38, v19, v38
	v_add_f32_e32 v39, v24, v39
	v_exp_f32_e32 v33, v33
	v_mul_f32_e32 v30, 0x3fb8aa3b, v30
	v_add_f32_e32 v40, v27, v40
	v_add_f32_e32 v38, v20, v38
	v_add_f32_e32 v39, v25, v39
	v_add_f32_e32 v42, 0, v36
	v_exp_f32_e32 v30, v30
	v_add_f32_e32 v38, v21, v38
	v_add_f32_e32 v39, v22, v39
	v_add_f32_e32 v40, v28, v40
	v_add_f32_e32 v41, v31, v42
	v_add_f32_e32 v38, v18, v38
	v_rcp_f32_e32 v39, v39
	v_add_f32_e32 v40, v29, v40
	v_add_f32_e32 v41, v32, v41
	v_rcp_f32_e32 v38, v38
	v_add_f32_e32 v40, v26, v40
	v_add_f32_e32 v41, v33, v41
	v_rcp_f32_e32 v40, v40
	v_add_f32_e32 v41, v30, v41
	v_rcp_f32_e32 v41, v41
	v_mul_f32_e32 v34, v34, v39
	v_mul_f32_e32 v23, v23, v39
	v_fmac_f32_e32 v34, v37, v38
	v_fmac_f32_e32 v23, v19, v38
	v_mul_f32_e32 v24, v24, v39
	v_fmac_f32_e32 v34, v35, v40
	v_fmac_f32_e32 v23, v27, v40
	v_mul_f32_e32 v22, v22, v39
	v_mul_f32_e32 v29, v29, v40
	v_fmac_f32_e32 v34, v36, v41
	v_fmac_f32_e32 v23, v31, v41
	v_fmac_f32_e32 v24, v20, v38
	v_fmac_f32_e32 v24, v28, v40
	v_cndmask_b32_e64 v20, v22, v34, s[4:5]
	v_cndmask_b32_e64 v22, v29, v23, s[4:5]
	v_mul_f32_e32 v21, v21, v38
	v_mul_f32_e32 v18, v18, v38
	v_mul_f32_e32 v25, v25, v39
	v_mul_f32_e32 v26, v26, v40
	v_mul_f32_e32 v33, v33, v41
	v_mul_f32_e32 v30, v30, v41
	v_fmac_f32_e32 v24, v32, v41
	v_mul_f32_e32 v20, 0x3e800000, v20
	v_mul_f32_e32 v22, 0x3e800000, v22
	v_mul_f32_e32 v19, 0x3e800000, v25
	ds_write2st64_b32 v222, v20, v22 offset1:8
	v_cndmask_b32_e64 v20, v26, v24, s[4:5]
	v_cndmask_b32_e64 v21, v33, v21, s[4:5]
	v_cndmask_b32_e64 v18, v30, v18, s[4:5]
	v_mul_f32_e32 v20, 0x3e800000, v20
	v_mul_f32_e32 v21, 0x3e800000, v21
	v_mul_f32_e32 v18, 0x3e800000, v18
	v_cndmask_b32_e64 v19, 0, v19, s[4:5]
	ds_write2st64_b32 v222, v20, v21 offset0:16 offset1:24
	ds_write2st64_b32 v222, v18, v19 offset0:32 offset1:40
	s_mul_hi_u32 s14, s62, 0x1b0000
	s_add_u32 s12, s44, s12
	v_mov_b64_e32 v[64:65], v[16:17]
	v_mov_b64_e32 v[48:49], v[16:17]
	v_mov_b64_e32 v[32:33], v[16:17]
	s_addc_u32 s16, s45, s14
	s_mov_b32 s17, 0
	v_mov_b64_e32 v[62:63], v[14:15]
	v_mov_b64_e32 v[60:61], v[12:13]
	v_mov_b64_e32 v[58:59], v[10:11]
	v_mov_b64_e32 v[56:57], v[8:9]
	v_mov_b64_e32 v[54:55], v[6:7]
	v_mov_b64_e32 v[52:53], v[4:5]
	v_mov_b64_e32 v[50:51], v[2:3]
	v_mov_b64_e32 v[46:47], v[14:15]
	v_mov_b64_e32 v[44:45], v[12:13]
	v_mov_b64_e32 v[42:43], v[10:11]
	v_mov_b64_e32 v[40:41], v[8:9]
	v_mov_b64_e32 v[38:39], v[6:7]
	v_mov_b64_e32 v[36:37], v[4:5]
	v_mov_b64_e32 v[34:35], v[2:3]
	v_mov_b64_e32 v[30:31], v[14:15]
	v_mov_b64_e32 v[28:29], v[12:13]
	v_mov_b64_e32 v[26:27], v[10:11]
	v_mov_b64_e32 v[24:25], v[8:9]
	v_mov_b64_e32 v[22:23], v[6:7]
	v_mov_b64_e32 v[20:21], v[4:5]
	v_mov_b64_e32 v[18:19], v[2:3]
	s_mov_b32 s18, 0
	s_mul_i32 s25, s33, 0x9000
	s_add_i32 s26, s33, -1
	s_cmp_eq_u32 s33, 0
	s_cselect_b32 s26, 2, s26
	s_mul_i32 s26, s26, 0x9000
	s_cmp_lg_u32 s4, 0
	s_cselect_b32 s27, 0x7fffffff, 40
	v_readfirstlane_b32 s28, v0
	s_lshl_b32 s28, s28, 4
	s_and_b32 s29, s28, 0xfffff000
	s_and_b32 s28, s28, 0xfffffc00
	s_add_i32 s28, s28, 0x8000
	s_sub_i32 s29, 0x8000, s29
	s_branch .LBB1_10

.LBB1_15:
	v_add_u32_e32 v240, s25, v247
	ds_read_b128 v[130:133], v189 offset:32768
	ds_read_b128 v[134:137], v189 offset:32800
	ds_read_b128 v[138:141], v189 offset:32832
	ds_read_b128 v[142:145], v189 offset:32864
	ds_read_b128 v[190:193], v240 offset:32768
	ds_read_b128 v[194:197], v240 offset:33792
	ds_read_b128 v[198:201], v240 offset:34816
	ds_read_b128 v[202:205], v240 offset:35840
	ds_read_b128 v[212:215], v240 offset:36864
	ds_read_b128 v[228:231], v240 offset:37888
	ds_read_b128 v[232:235], v240 offset:38912
	ds_read_b128 v[236:239], v240 offset:39936
	s_waitcnt lgkmcnt(7)
	v_mfma_f32_32x32x16_f16 v[130:145], v[190:193], v[146:149], v[130:145]
	s_waitcnt lgkmcnt(6)
	v_mfma_f32_32x32x16_f16 v[130:145], v[194:197], v[150:153], v[130:145]
	s_waitcnt lgkmcnt(5)
	v_mfma_f32_32x32x16_f16 v[130:145], v[198:201], v[154:157], v[130:145]
	s_waitcnt lgkmcnt(4)
	v_mfma_f32_32x32x16_f16 v[130:145], v[202:205], v[158:161], v[130:145]
	s_add_i32 s23, s26, s28
	s_add_i32 m0, s23, 0x0
	s_add_u32 s20, s12, 0x12000
	s_addc_u32 s21, s16, 0
	global_load_lds_dwordx4 v226, s[20:21]
	s_waitcnt lgkmcnt(3)
	v_mfma_f32_32x32x16_f16 v[130:145], v[212:215], v[162:165], v[130:145]
	s_add_i32 m0, s23, 0x2000
	s_add_u32 s20, s12, 0x14000
	s_addc_u32 s21, s16, 0
	global_load_lds_dwordx4 v226, s[20:21]
	s_waitcnt lgkmcnt(2)
	v_mfma_f32_32x32x16_f16 v[130:145], v[228:231], v[166:169], v[130:145]
	s_add_i32 m0, s23, 0x4000
	s_add_u32 s20, s12, 0x16000
	s_addc_u32 s21, s16, 0
	global_load_lds_dwordx4 v226, s[20:21]
	s_waitcnt lgkmcnt(1)
	v_mfma_f32_32x32x16_f16 v[130:145], v[232:235], v[170:173], v[130:145]
	s_add_i32 m0, s23, 0x6000
	s_add_u32 s20, s12, 0x18000
	s_addc_u32 s21, s16, 0
	global_load_lds_dwordx4 v226, s[20:21]
	s_waitcnt lgkmcnt(0)
	v_mfma_f32_32x32x16_f16 v[130:145], v[236:239], v[174:177], v[130:145]
	s_add_i32 m0, s23, s29
	s_add_u32 s20, s12, 0x1a000
	s_addc_u32 s21, s16, 0
	global_load_lds_dwordx4 v224, s[20:21]
	ds_read_b128 v[190:193], v240 offset:40960
	ds_read_b128 v[194:197], v240 offset:41984
	ds_read_b128 v[198:201], v240 offset:43008
	ds_read_b128 v[202:205], v240 offset:44032
	ds_read_b128 v[212:215], v240 offset:45056
	ds_read_b128 v[228:231], v240 offset:46080
	ds_read_b128 v[232:235], v240 offset:47104
	ds_read_b128 v[236:239], v240 offset:48128
	v_cvt_pk_f16_f32 v130, v130, v131
	v_cvt_pk_f16_f32 v131, v132, v133
	v_cvt_pk_f16_f32 v132, v134, v135
	v_cvt_pk_f16_f32 v133, v136, v137
	v_and_b32_e32 v134, 0x7fff7fff, v130
	v_and_b32_e32 v135, 0x7fff7fff, v131
	v_and_b32_e32 v136, 0x7fff7fff, v132
	v_and_b32_e32 v137, 0x7fff7fff, v133
	v_pk_min_f16 v134, v134, v186
	v_pk_min_f16 v135, v135, v186
	v_pk_min_f16 v136, v136, v186
	v_pk_min_f16 v137, v137, v186
	v_pk_max_f16 v130, v130, v187
	v_pk_max_f16 v131, v131, v187
	s_nop 0
	v_pk_fma_f16 v134, v134, s53, -1.0 op_sel_hi:[1,0,0]
	v_pk_fma_f16 v135, v135, s53, -1.0 op_sel_hi:[1,0,0]
	v_pk_fma_f16 v136, v136, s53, -1.0 op_sel_hi:[1,0,0]
	v_pk_fma_f16 v137, v137, s53, -1.0 op_sel_hi:[1,0,0]
	v_pk_fma_f16 v240, v134, s54, v188 op_sel_hi:[1,0,0]
	v_pk_fma_f16 v241, v135, s54, v188 op_sel_hi:[1,0,0]
	v_pk_fma_f16 v242, v136, s54, v188 op_sel_hi:[1,0,0]
	v_pk_fma_f16 v243, v137, s54, v188 op_sel_hi:[1,0,0]
	v_pk_fma_f16 v240, v134, v240, s55 op_sel_hi:[1,1,0]
	v_pk_fma_f16 v241, v135, v241, s55 op_sel_hi:[1,1,0]
	v_pk_fma_f16 v242, v136, v242, s55 op_sel_hi:[1,1,0]
	v_pk_fma_f16 v243, v137, v243, s55 op_sel_hi:[1,1,0]
	v_pk_fma_f16 v240, v134, v240, s56 op_sel_hi:[1,1,0]
	v_pk_fma_f16 v241, v135, v241, s56 op_sel_hi:[1,1,0]
	v_pk_fma_f16 v242, v136, v242, s56 op_sel_hi:[1,1,0]
	v_pk_fma_f16 v243, v137, v243, s56 op_sel_hi:[1,1,0]
	v_pk_fma_f16 v240, v134, v240, s57 op_sel_hi:[1,1,0]
	v_pk_fma_f16 v241, v135, v241, s57 op_sel_hi:[1,1,0]
	v_pk_fma_f16 v242, v136, v242, s57 op_sel_hi:[1,1,0]
	v_pk_fma_f16 v243, v137, v243, s57 op_sel_hi:[1,1,0]
	v_pk_fma_f16 v240, v134, v240, s58 op_sel_hi:[1,1,0]
	v_pk_fma_f16 v241, v135, v241, s58 op_sel_hi:[1,1,0]
	v_pk_fma_f16 v242, v136, v242, s58 op_sel_hi:[1,1,0]
	v_pk_fma_f16 v243, v137, v243, s58 op_sel_hi:[1,1,0]
	v_pk_fma_f16 v240, v134, v240, s59 op_sel_hi:[1,1,0]
	v_pk_fma_f16 v241, v135, v241, s59 op_sel_hi:[1,1,0]
	v_pk_fma_f16 v242, v136, v242, s59 op_sel_hi:[1,1,0]
	v_pk_fma_f16 v243, v137, v243, s59 op_sel_hi:[1,1,0]
	v_pk_max_f16 v132, v132, v187
	v_pk_max_f16 v133, v133, v187
	v_pk_fma_f16 v134, v134, v240, s60 op_sel_hi:[1,1,0]
	v_pk_fma_f16 v135, v135, v241, s60 op_sel_hi:[1,1,0]
	v_pk_fma_f16 v136, v136, v242, s60 op_sel_hi:[1,1,0]
	v_pk_fma_f16 v137, v137, v243, s60 op_sel_hi:[1,1,0]
	v_pk_add_f16 v130, v130, v134
	v_pk_add_f16 v131, v131, v135
	v_pk_add_f16 v132, v132, v136
	v_pk_add_f16 v133, v133, v137
	v_cvt_pk_f16_f32 v134, v138, v139
	v_cvt_pk_f16_f32 v135, v140, v141
	v_cvt_pk_f16_f32 v136, v142, v143
	v_cvt_pk_f16_f32 v137, v144, v145
	v_and_b32_e32 v138, 0x7fff7fff, v134
	v_and_b32_e32 v139, 0x7fff7fff, v135
	v_and_b32_e32 v140, 0x7fff7fff, v136
	v_and_b32_e32 v141, 0x7fff7fff, v137
	v_pk_min_f16 v138, v138, v186
	v_pk_min_f16 v139, v139, v186
	v_pk_min_f16 v140, v140, v186
	v_pk_min_f16 v141, v141, v186
	s_waitcnt lgkmcnt(7)
	v_mfma_f32_32x32x16_f16 v[66:81], v[190:193], v[130:133], v[66:81]
	v_pk_fma_f16 v138, v138, s53, -1.0 op_sel_hi:[1,0,0]
	v_pk_fma_f16 v139, v139, s53, -1.0 op_sel_hi:[1,0,0]
	v_pk_fma_f16 v140, v140, s53, -1.0 op_sel_hi:[1,0,0]
	v_pk_fma_f16 v141, v141, s53, -1.0 op_sel_hi:[1,0,0]
	v_pk_fma_f16 v142, v138, s54, v188 op_sel_hi:[1,0,0]
	v_pk_fma_f16 v143, v139, s54, v188 op_sel_hi:[1,0,0]
	v_pk_fma_f16 v144, v140, s54, v188 op_sel_hi:[1,0,0]
	v_pk_fma_f16 v145, v141, s54, v188 op_sel_hi:[1,0,0]
	s_waitcnt lgkmcnt(5)
	v_mfma_f32_32x32x16_f16 v[82:97], v[198:201], v[130:133], v[82:97]
	v_pk_fma_f16 v142, v138, v142, s55 op_sel_hi:[1,1,0]
	v_pk_fma_f16 v143, v139, v143, s55 op_sel_hi:[1,1,0]
	v_pk_fma_f16 v144, v140, v144, s55 op_sel_hi:[1,1,0]
	v_pk_fma_f16 v145, v141, v145, s55 op_sel_hi:[1,1,0]
	v_pk_fma_f16 v142, v138, v142, s56 op_sel_hi:[1,1,0]
	v_pk_fma_f16 v143, v139, v143, s56 op_sel_hi:[1,1,0]
	v_pk_fma_f16 v144, v140, v144, s56 op_sel_hi:[1,1,0]
	s_waitcnt lgkmcnt(3)
	v_mfma_f32_32x32x16_f16 v[98:113], v[212:215], v[130:133], v[98:113]
	v_pk_fma_f16 v145, v141, v145, s56 op_sel_hi:[1,1,0]
	v_pk_fma_f16 v142, v138, v142, s57 op_sel_hi:[1,1,0]
	v_pk_fma_f16 v143, v139, v143, s57 op_sel_hi:[1,1,0]
	v_pk_fma_f16 v144, v140, v144, s57 op_sel_hi:[1,1,0]
	v_pk_fma_f16 v145, v141, v145, s57 op_sel_hi:[1,1,0]
	v_pk_fma_f16 v142, v138, v142, s58 op_sel_hi:[1,1,0]
	v_pk_fma_f16 v143, v139, v143, s58 op_sel_hi:[1,1,0]
	s_waitcnt lgkmcnt(1)
	v_mfma_f32_32x32x16_f16 v[114:129], v[232:235], v[130:133], v[114:129]
	v_pk_fma_f16 v144, v140, v144, s58 op_sel_hi:[1,1,0]
	v_pk_fma_f16 v145, v141, v145, s58 op_sel_hi:[1,1,0]
	v_pk_fma_f16 v142, v138, v142, s59 op_sel_hi:[1,1,0]
	v_pk_fma_f16 v143, v139, v143, s59 op_sel_hi:[1,1,0]
	v_pk_fma_f16 v144, v140, v144, s59 op_sel_hi:[1,1,0]
	v_pk_fma_f16 v145, v141, v145, s59 op_sel_hi:[1,1,0]
	v_pk_max_f16 v134, v134, v187
	v_pk_max_f16 v135, v135, v187
	v_pk_max_f16 v136, v136, v187
	v_pk_max_f16 v137, v137, v187
	v_pk_fma_f16 v138, v138, v142, s60 op_sel_hi:[1,1,0]
	v_pk_fma_f16 v139, v139, v143, s60 op_sel_hi:[1,1,0]
	v_pk_fma_f16 v140, v140, v144, s60 op_sel_hi:[1,1,0]
	v_pk_fma_f16 v141, v141, v145, s60 op_sel_hi:[1,1,0]
	v_pk_add_f16 v134, v134, v138
	v_pk_add_f16 v135, v135, v139
	v_pk_add_f16 v136, v136, v140
	v_pk_add_f16 v137, v137, v141
	s_cmp_lg_u32 s19, 7
	s_nop 0
	v_mfma_f32_32x32x16_f16 v[66:81], v[194:197], v[134:137], v[66:81]
	v_mfma_f32_32x32x16_f16 v[82:97], v[202:205], v[134:137], v[82:97]
	v_mfma_f32_32x32x16_f16 v[98:113], v[228:231], v[134:137], v[98:113]
	s_waitcnt lgkmcnt(0)
	v_mfma_f32_32x32x16_f16 v[114:129], v[236:239], v[134:137], v[114:129]
	s_cbranch_scc1 .LBB1_17
	ds_read_b128 v[132:135], v189 offset:33312
	ds_read_b128 v[136:139], v189 offset:33344
	ds_read_b128 v[140:143], v189 offset:33824
	ds_read_b128 v[190:193], v189 offset:33856
	ds_read_b128 v[194:197], v189 offset:33792
	ds_read_b128 v[198:201], v189 offset:33376
	ds_read_b128 v[202:205], v189 offset:33888
	s_lshl_b32 s19, s18, 6
	s_and_b32 s19, s19, 0xe00
	v_lshl_add_u32 v130, s19, 2, v222
	ds_read_b128 v[212:215], v189 offset:33280
	ds_read_b32 v130, v130
	v_pk_add_f32 v[144:145], v[66:67], v[68:69]
	v_pk_mul_f32 v[228:229], v[66:67], v[66:67]
	v_pk_add_f32 v[230:231], v[82:83], v[84:85]
	v_pk_mul_f32 v[232:233], v[82:83], v[82:83]
	v_pk_add_f32 v[234:235], v[98:99], v[100:101]
	v_pk_mul_f32 v[236:237], v[98:99], v[98:99]
	v_pk_add_f32 v[238:239], v[114:115], v[116:117]
	v_pk_mul_f32 v[240:241], v[114:115], v[114:115]
	v_pk_fma_f32 v[228:229], v[68:69], v[68:69], v[228:229]
	v_pk_fma_f32 v[232:233], v[84:85], v[84:85], v[232:233]
	v_pk_fma_f32 v[236:237], v[100:101], v[100:101], v[236:237]
	v_pk_fma_f32 v[240:241], v[116:117], v[116:117], v[240:241]
	v_pk_add_f32 v[144:145], v[70:71], v[144:145]
	v_pk_add_f32 v[230:231], v[86:87], v[230:231]
	v_pk_add_f32 v[234:235], v[102:103], v[234:235]
	v_pk_add_f32 v[238:239], v[118:119], v[238:239]
	v_pk_fma_f32 v[228:229], v[70:71], v[70:71], v[228:229]
	v_pk_fma_f32 v[232:233], v[86:87], v[86:87], v[232:233]
	v_pk_fma_f32 v[236:237], v[102:103], v[102:103], v[236:237]
	v_pk_fma_f32 v[240:241], v[118:119], v[118:119], v[240:241]
	v_pk_add_f32 v[144:145], v[72:73], v[144:145]
	v_pk_add_f32 v[230:231], v[88:89], v[230:231]
	v_pk_add_f32 v[234:235], v[104:105], v[234:235]
	v_pk_add_f32 v[238:239], v[120:121], v[238:239]
	v_pk_fma_f32 v[228:229], v[72:73], v[72:73], v[228:229]
	v_pk_fma_f32 v[232:233], v[88:89], v[88:89], v[232:233]
	v_pk_fma_f32 v[236:237], v[104:105], v[104:105], v[236:237]
	v_pk_fma_f32 v[240:241], v[120:121], v[120:121], v[240:241]
	v_pk_add_f32 v[144:145], v[74:75], v[144:145]
	v_pk_add_f32 v[230:231], v[90:91], v[230:231]
	v_pk_add_f32 v[234:235], v[106:107], v[234:235]
	v_pk_add_f32 v[238:239], v[122:123], v[238:239]
	v_pk_fma_f32 v[228:229], v[74:75], v[74:75], v[228:229]
	v_pk_fma_f32 v[232:233], v[90:91], v[90:91], v[232:233]
	v_pk_fma_f32 v[236:237], v[106:107], v[106:107], v[236:237]
	v_pk_fma_f32 v[240:241], v[122:123], v[122:123], v[240:241]
	v_pk_add_f32 v[144:145], v[76:77], v[144:145]
	v_pk_add_f32 v[230:231], v[92:93], v[230:231]
	v_pk_add_f32 v[234:235], v[108:109], v[234:235]
	v_pk_add_f32 v[238:239], v[124:125], v[238:239]
	v_pk_fma_f32 v[228:229], v[76:77], v[76:77], v[228:229]
	v_pk_fma_f32 v[232:233], v[92:93], v[92:93], v[232:233]
	v_pk_fma_f32 v[236:237], v[108:109], v[108:109], v[236:237]
	v_pk_fma_f32 v[240:241], v[124:125], v[124:125], v[240:241]
	v_pk_add_f32 v[144:145], v[78:79], v[144:145]
	v_pk_add_f32 v[230:231], v[94:95], v[230:231]
	v_pk_add_f32 v[234:235], v[110:111], v[234:235]
	v_pk_add_f32 v[238:239], v[126:127], v[238:239]
	v_pk_fma_f32 v[228:229], v[78:79], v[78:79], v[228:229]
	v_pk_fma_f32 v[232:233], v[94:95], v[94:95], v[232:233]
	v_pk_fma_f32 v[236:237], v[110:111], v[110:111], v[236:237]
	v_pk_fma_f32 v[240:241], v[126:127], v[126:127], v[240:241]
	v_pk_add_f32 v[144:145], v[80:81], v[144:145]
	v_pk_add_f32 v[230:231], v[96:97], v[230:231]
	v_pk_add_f32 v[234:235], v[112:113], v[234:235]
	v_pk_add_f32 v[238:239], v[128:129], v[238:239]
	v_pk_fma_f32 v[228:229], v[80:81], v[80:81], v[228:229]
	v_pk_fma_f32 v[232:233], v[96:97], v[96:97], v[232:233]
	v_pk_fma_f32 v[236:237], v[112:113], v[112:113], v[236:237]
	v_pk_fma_f32 v[240:241], v[128:129], v[128:129], v[240:241]
	v_pk_add_f32 v[144:145], v[144:145], v[230:231]
	v_pk_add_f32 v[230:231], v[234:235], v[238:239]
	v_pk_add_f32 v[228:229], v[228:229], v[232:233]
	v_pk_add_f32 v[144:145], v[144:145], v[230:231]
	v_pk_add_f32 v[230:231], v[236:237], v[240:241]
	s_nop 0
	v_pk_add_f32 v[228:229], v[228:229], v[230:231]
	v_mov_b32_e32 v231, v144
	v_mov_b32_e32 v230, v228
	v_mov_b32_e32 v144, v229
	v_pk_add_f32 v[144:145], v[230:231], v[144:145]
	ds_bpermute_b32 v229, v225, v145
	ds_bpermute_b32 v228, v225, v144
	s_waitcnt lgkmcnt(0)
	v_pk_add_f32 v[144:145], v[144:145], v[228:229]
	s_nop 0
	v_pk_mul_f32 v[144:145], v[144:145], s[48:49] op_sel_hi:[1,0]
	s_nop 0
	v_fma_f32 v131, -v145, v145, v144
	v_add_f32_e32 v131, 0x3727c5ac, v131
	v_mul_f32_e32 v144, 0x4b800000, v131
	v_cmp_gt_f32_e32 vcc, s61, v131
	s_nop 1
	v_cndmask_b32_e32 v131, v131, v144, vcc
	v_rsq_f32_e32 v131, v131
	s_nop 0
	v_mul_f32_e32 v144, 0x45800000, v131
	v_cndmask_b32_e32 v144, v131, v144, vcc
	v_mul_f32_e64 v228, v144, -v145
	v_pk_fma_f32 v[230:231], v[80:81], v[144:145], v[228:229] op_sel_hi:[1,0,0]
	v_pk_fma_f32 v[232:233], v[78:79], v[144:145], v[228:229] op_sel_hi:[1,0,0]
	v_pk_fma_f32 v[234:235], v[76:77], v[144:145], v[228:229] op_sel_hi:[1,0,0]
	v_pk_fma_f32 v[236:237], v[74:75], v[144:145], v[228:229] op_sel_hi:[1,0,0]
	v_pk_fma_f32 v[238:239], v[72:73], v[144:145], v[228:229] op_sel_hi:[1,0,0]
	v_pk_fma_f32 v[240:241], v[70:71], v[144:145], v[228:229] op_sel_hi:[1,0,0]
	v_pk_fma_f32 v[242:243], v[68:69], v[144:145], v[228:229] op_sel_hi:[1,0,0]
	v_pk_fma_f32 v[244:245], v[66:67], v[144:145], v[228:229] op_sel_hi:[1,0,0]
	v_pk_fma_f32 v[196:197], v[242:243], v[214:215], v[196:197]
	v_pk_fma_f32 v[194:195], v[244:245], v[212:213], v[194:195]
	v_pk_fma_f32 v[132:133], v[240:241], v[132:133], v[140:141]
	v_pk_fma_f32 v[134:135], v[238:239], v[134:135], v[142:143]
	v_pk_fma_f32 v[136:137], v[236:237], v[136:137], v[190:191]
	v_pk_fma_f32 v[138:139], v[234:235], v[138:139], v[192:193]
	v_pk_fma_f32 v[140:141], v[232:233], v[198:199], v[202:203]
	v_pk_fma_f32 v[142:143], v[230:231], v[200:201], v[204:205]
	v_pk_fma_f32 v[14:15], v[130:131], v[140:141], v[14:15] op_sel_hi:[0,1,1]
	v_pk_fma_f32 v[16:17], v[130:131], v[142:143], v[16:17] op_sel_hi:[0,1,1]
	v_pk_fma_f32 v[12:13], v[130:131], v[138:139], v[12:13] op_sel_hi:[0,1,1]
	v_pk_fma_f32 v[10:11], v[130:131], v[136:137], v[10:11] op_sel_hi:[0,1,1]
	v_pk_fma_f32 v[8:9], v[130:131], v[134:135], v[8:9] op_sel_hi:[0,1,1]
	v_pk_fma_f32 v[6:7], v[130:131], v[132:133], v[6:7] op_sel_hi:[0,1,1]
	v_pk_fma_f32 v[4:5], v[130:131], v[196:197], v[4:5] op_sel_hi:[0,1,1]
	v_pk_fma_f32 v[2:3], v[130:131], v[194:195], v[2:3] op_sel_hi:[0,1,1]
	ds_read_b128 v[132:135], v189 offset:33408
	ds_read_b128 v[136:139], v189 offset:33440
	ds_read_b128 v[140:143], v189 offset:33920
	ds_read_b128 v[190:193], v189 offset:33952
	ds_read_b128 v[194:197], v189 offset:33472
	ds_read_b128 v[198:201], v189 offset:33504
	ds_read_b128 v[202:205], v189 offset:33984
	ds_read_b128 v[212:215], v189 offset:34016
	v_pk_fma_f32 v[230:231], v[96:97], v[144:145], v[228:229] op_sel_hi:[1,0,0]
	v_pk_fma_f32 v[232:233], v[94:95], v[144:145], v[228:229] op_sel_hi:[1,0,0]
	v_pk_fma_f32 v[234:235], v[92:93], v[144:145], v[228:229] op_sel_hi:[1,0,0]
	v_pk_fma_f32 v[236:237], v[90:91], v[144:145], v[228:229] op_sel_hi:[1,0,0]
	v_pk_fma_f32 v[238:239], v[88:89], v[144:145], v[228:229] op_sel_hi:[1,0,0]
	v_pk_fma_f32 v[240:241], v[86:87], v[144:145], v[228:229] op_sel_hi:[1,0,0]
	v_pk_fma_f32 v[242:243], v[84:85], v[144:145], v[228:229] op_sel_hi:[1,0,0]
	v_pk_fma_f32 v[244:245], v[82:83], v[144:145], v[228:229] op_sel_hi:[1,0,0]
	s_waitcnt lgkmcnt(5)
	v_pk_fma_f32 v[134:135], v[242:243], v[134:135], v[142:143]
	v_pk_fma_f32 v[132:133], v[244:245], v[132:133], v[140:141]
	s_waitcnt lgkmcnt(4)
	v_pk_fma_f32 v[136:137], v[240:241], v[136:137], v[190:191]
	v_pk_fma_f32 v[138:139], v[238:239], v[138:139], v[192:193]
	s_waitcnt lgkmcnt(1)
	v_pk_fma_f32 v[140:141], v[236:237], v[194:195], v[202:203]
	v_pk_fma_f32 v[142:143], v[234:235], v[196:197], v[204:205]
	s_waitcnt lgkmcnt(0)
	v_pk_fma_f32 v[190:191], v[232:233], v[198:199], v[212:213]
	v_pk_fma_f32 v[192:193], v[230:231], v[200:201], v[214:215]
	v_pk_fma_f32 v[62:63], v[130:131], v[190:191], v[62:63] op_sel_hi:[0,1,1]
	v_pk_fma_f32 v[64:65], v[130:131], v[192:193], v[64:65] op_sel_hi:[0,1,1]
	v_pk_fma_f32 v[60:61], v[130:131], v[142:143], v[60:61] op_sel_hi:[0,1,1]
	v_pk_fma_f32 v[58:59], v[130:131], v[140:141], v[58:59] op_sel_hi:[0,1,1]
	v_pk_fma_f32 v[56:57], v[130:131], v[138:139], v[56:57] op_sel_hi:[0,1,1]
	v_pk_fma_f32 v[54:55], v[130:131], v[136:137], v[54:55] op_sel_hi:[0,1,1]
	v_pk_fma_f32 v[52:53], v[130:131], v[134:135], v[52:53] op_sel_hi:[0,1,1]
	v_pk_fma_f32 v[50:51], v[130:131], v[132:133], v[50:51] op_sel_hi:[0,1,1]
	ds_read_b128 v[132:135], v189 offset:33536
	ds_read_b128 v[136:139], v189 offset:33568
	ds_read_b128 v[140:143], v189 offset:34048
	ds_read_b128 v[190:193], v189 offset:34080
	ds_read_b128 v[194:197], v189 offset:33600
	ds_read_b128 v[198:201], v189 offset:33632
	ds_read_b128 v[202:205], v189 offset:34112
	ds_read_b128 v[212:215], v189 offset:34144
	v_pk_fma_f32 v[230:231], v[112:113], v[144:145], v[228:229] op_sel_hi:[1,0,0]
	v_pk_fma_f32 v[232:233], v[110:111], v[144:145], v[228:229] op_sel_hi:[1,0,0]
	v_pk_fma_f32 v[234:235], v[108:109], v[144:145], v[228:229] op_sel_hi:[1,0,0]
	v_pk_fma_f32 v[236:237], v[106:107], v[144:145], v[228:229] op_sel_hi:[1,0,0]
	v_pk_fma_f32 v[238:239], v[104:105], v[144:145], v[228:229] op_sel_hi:[1,0,0]
	v_pk_fma_f32 v[240:241], v[102:103], v[144:145], v[228:229] op_sel_hi:[1,0,0]
	v_pk_fma_f32 v[242:243], v[100:101], v[144:145], v[228:229] op_sel_hi:[1,0,0]
	v_pk_fma_f32 v[244:245], v[98:99], v[144:145], v[228:229] op_sel_hi:[1,0,0]
	s_waitcnt lgkmcnt(5)
	v_pk_fma_f32 v[134:135], v[242:243], v[134:135], v[142:143]
	v_pk_fma_f32 v[132:133], v[244:245], v[132:133], v[140:141]
	s_waitcnt lgkmcnt(4)
	v_pk_fma_f32 v[136:137], v[240:241], v[136:137], v[190:191]
	v_pk_fma_f32 v[138:139], v[238:239], v[138:139], v[192:193]
	s_waitcnt lgkmcnt(1)
	v_pk_fma_f32 v[140:141], v[236:237], v[194:195], v[202:203]
	v_pk_fma_f32 v[142:143], v[234:235], v[196:197], v[204:205]
	s_waitcnt lgkmcnt(0)
	v_pk_fma_f32 v[190:191], v[232:233], v[198:199], v[212:213]
	v_pk_fma_f32 v[192:193], v[230:231], v[200:201], v[214:215]
	v_pk_fma_f32 v[46:47], v[130:131], v[190:191], v[46:47] op_sel_hi:[0,1,1]
	v_pk_fma_f32 v[48:49], v[130:131], v[192:193], v[48:49] op_sel_hi:[0,1,1]
	v_pk_fma_f32 v[44:45], v[130:131], v[142:143], v[44:45] op_sel_hi:[0,1,1]
	v_pk_fma_f32 v[42:43], v[130:131], v[140:141], v[42:43] op_sel_hi:[0,1,1]
	v_pk_fma_f32 v[40:41], v[130:131], v[138:139], v[40:41] op_sel_hi:[0,1,1]
	v_pk_fma_f32 v[38:39], v[130:131], v[136:137], v[38:39] op_sel_hi:[0,1,1]
	v_pk_fma_f32 v[36:37], v[130:131], v[134:135], v[36:37] op_sel_hi:[0,1,1]
	v_pk_fma_f32 v[34:35], v[130:131], v[132:133], v[34:35] op_sel_hi:[0,1,1]
	ds_read_b128 v[132:135], v189 offset:33664
	ds_read_b128 v[136:139], v189 offset:33696
	ds_read_b128 v[140:143], v189 offset:34176
	ds_read_b128 v[190:193], v189 offset:34208
	ds_read_b128 v[194:197], v189 offset:33728
	ds_read_b128 v[198:201], v189 offset:33760
	ds_read_b128 v[202:205], v189 offset:34240
	ds_read_b128 v[212:215], v189 offset:34272
	v_pk_fma_f32 v[230:231], v[128:129], v[144:145], v[228:229] op_sel_hi:[1,0,0]
	v_pk_fma_f32 v[232:233], v[126:127], v[144:145], v[228:229] op_sel_hi:[1,0,0]
	v_pk_fma_f32 v[234:235], v[124:125], v[144:145], v[228:229] op_sel_hi:[1,0,0]
	v_pk_fma_f32 v[236:237], v[122:123], v[144:145], v[228:229] op_sel_hi:[1,0,0]
	v_pk_fma_f32 v[238:239], v[120:121], v[144:145], v[228:229] op_sel_hi:[1,0,0]
	v_pk_fma_f32 v[240:241], v[118:119], v[144:145], v[228:229] op_sel_hi:[1,0,0]
	v_pk_fma_f32 v[242:243], v[116:117], v[144:145], v[228:229] op_sel_hi:[1,0,0]
	v_pk_fma_f32 v[144:145], v[114:115], v[144:145], v[228:229] op_sel_hi:[1,0,0]
	s_waitcnt lgkmcnt(5)
	v_pk_fma_f32 v[134:135], v[242:243], v[134:135], v[142:143]
	v_pk_fma_f32 v[132:133], v[144:145], v[132:133], v[140:141]
	s_waitcnt lgkmcnt(4)
	v_pk_fma_f32 v[136:137], v[240:241], v[136:137], v[190:191]
	v_pk_fma_f32 v[138:139], v[238:239], v[138:139], v[192:193]
	s_waitcnt lgkmcnt(1)
	v_pk_fma_f32 v[140:141], v[236:237], v[194:195], v[202:203]
	v_pk_fma_f32 v[142:143], v[234:235], v[196:197], v[204:205]
	s_waitcnt lgkmcnt(0)
	v_pk_fma_f32 v[144:145], v[232:233], v[198:199], v[212:213]
	v_pk_fma_f32 v[190:191], v[230:231], v[200:201], v[214:215]
	v_pk_fma_f32 v[30:31], v[130:131], v[144:145], v[30:31] op_sel_hi:[0,1,1]
	v_pk_fma_f32 v[32:33], v[130:131], v[190:191], v[32:33] op_sel_hi:[0,1,1]
	v_pk_fma_f32 v[28:29], v[130:131], v[142:143], v[28:29] op_sel_hi:[0,1,1]
	v_pk_fma_f32 v[26:27], v[130:131], v[140:141], v[26:27] op_sel_hi:[0,1,1]
	v_pk_fma_f32 v[24:25], v[130:131], v[138:139], v[24:25] op_sel_hi:[0,1,1]
	v_pk_fma_f32 v[22:23], v[130:131], v[136:137], v[22:23] op_sel_hi:[0,1,1]
	v_pk_fma_f32 v[20:21], v[130:131], v[134:135], v[20:21] op_sel_hi:[0,1,1]
	v_pk_fma_f32 v[18:19], v[130:131], v[132:133], v[18:19] op_sel_hi:[0,1,1]

.LBB1_23:
	v_add_co_u32_e32 v26, vcc, 0x2dc000, v210
	s_mov_b32 s12, 0x2dd000
	s_nop 0
	v_addc_co_u32_e32 v27, vcc, 0, v211, vcc
	global_load_dwordx4 v[2:5], v[26:27], off
	global_load_dwordx4 v[18:21], v[26:27], off offset:1024
	global_load_dwordx4 v[22:25], v[26:27], off offset:2048
	s_mov_b32 s40, 0
	v_mov_b32_e32 v228, 0
	s_movk_i32 s41, 0x31f0
	s_mov_b32 s42, 0xab4a
	s_mov_b32 s43, 0x800000
	v_mov_b32_e32 v229, 0x43804380
	v_mov_b32_e32 v230, 0xac0d
	v_mov_b32_e32 v87, 0
	v_mov_b32_e32 v86, 0
	v_mov_b32_e32 v85, 0
	v_mov_b32_e32 v84, 0
	v_mov_b32_e32 v91, 0
	v_mov_b32_e32 v90, 0
	v_mov_b32_e32 v89, 0
	v_mov_b32_e32 v88, 0
	v_mov_b32_e32 v95, 0
	v_mov_b32_e32 v94, 0
	v_mov_b32_e32 v93, 0
	v_mov_b32_e32 v92, 0
	v_mov_b32_e32 v99, 0
	v_mov_b32_e32 v98, 0
	v_mov_b32_e32 v97, 0
	v_mov_b32_e32 v96, 0
	v_mov_b32_e32 v103, 0
	v_mov_b32_e32 v102, 0
	v_mov_b32_e32 v101, 0
	v_mov_b32_e32 v100, 0
	v_mov_b32_e32 v107, 0
	v_mov_b32_e32 v106, 0
	v_mov_b32_e32 v105, 0
	v_mov_b32_e32 v104, 0
	v_mov_b32_e32 v111, 0
	v_mov_b32_e32 v110, 0
	v_mov_b32_e32 v109, 0
	v_mov_b32_e32 v108, 0
	v_mov_b32_e32 v115, 0
	v_mov_b32_e32 v114, 0
	v_mov_b32_e32 v113, 0
	v_mov_b32_e32 v112, 0
	v_mov_b32_e32 v119, 0
	v_mov_b32_e32 v118, 0
	v_mov_b32_e32 v117, 0
	v_mov_b32_e32 v116, 0
	v_mov_b32_e32 v123, 0
	v_mov_b32_e32 v122, 0
	v_mov_b32_e32 v121, 0
	v_mov_b32_e32 v120, 0
	v_mov_b32_e32 v127, 0
	v_mov_b32_e32 v126, 0
	v_mov_b32_e32 v125, 0
	v_mov_b32_e32 v124, 0
	v_mov_b32_e32 v131, 0
	v_mov_b32_e32 v130, 0
	v_mov_b32_e32 v129, 0
	v_mov_b32_e32 v128, 0
	v_mov_b32_e32 v135, 0
	v_mov_b32_e32 v134, 0
	v_mov_b32_e32 v133, 0
	v_mov_b32_e32 v132, 0
	v_mov_b32_e32 v139, 0
	v_mov_b32_e32 v138, 0
	v_mov_b32_e32 v137, 0
	v_mov_b32_e32 v136, 0
	v_mov_b32_e32 v143, 0
	v_mov_b32_e32 v142, 0
	v_mov_b32_e32 v141, 0
	v_mov_b32_e32 v140, 0
	v_mov_b32_e32 v189, 0
	v_mov_b32_e32 v188, 0
	v_mov_b32_e32 v187, 0
	v_mov_b32_e32 v186, 0
	s_waitcnt vmcnt(2) lgkmcnt(7)
	v_mfma_f32_32x32x16_f16 v[2:17], v[2:5], v[146:149], 0
	s_waitcnt vmcnt(1) lgkmcnt(6)
	v_mfma_f32_32x32x16_f16 v[2:17], v[18:21], v[150:153], v[2:17]
	global_load_dwordx4 v[18:21], v[26:27], off offset:3072
	v_add_co_u32_e32 v26, vcc, s12, v210
	s_nop 1
	v_addc_co_u32_e32 v27, vcc, 0, v211, vcc
	s_waitcnt vmcnt(1) lgkmcnt(5)
	v_mfma_f32_32x32x16_f16 v[2:17], v[22:25], v[154:157], v[2:17]
	global_load_dwordx4 v[22:25], v[26:27], off
	s_waitcnt vmcnt(1) lgkmcnt(4)
	v_mfma_f32_32x32x16_f16 v[2:17], v[18:21], v[158:161], v[2:17]
	global_load_dwordx4 v[18:21], v[26:27], off offset:1024
	s_waitcnt vmcnt(1) lgkmcnt(3)
	v_mfma_f32_32x32x16_f16 v[2:17], v[22:25], v[162:165], v[2:17]
	global_load_dwordx4 v[22:25], v[26:27], off offset:2048
	s_waitcnt vmcnt(1) lgkmcnt(2)
	v_mfma_f32_32x32x16_f16 v[2:17], v[18:21], v[166:169], v[2:17]
	global_load_dwordx4 v[18:21], v[26:27], off offset:3072
	s_load_dwordx16 s[12:27], s[10:11], 0x50
	s_load_dwordx4 s[28:31], s[10:11], 0x90
	v_cmp_eq_u32_e64 s[10:11], 0, v0
	s_waitcnt vmcnt(1) lgkmcnt(0)
	v_mfma_f32_32x32x16_f16 v[2:17], v[22:25], v[170:173], v[2:17]
	s_waitcnt vmcnt(0)
	v_mfma_f32_32x32x16_f16 v[2:17], v[18:21], v[174:177], v[2:17]
	s_nop 11
	ds_bpermute_b32 v18, v225, v2
	ds_bpermute_b32 v19, v225, v3
	ds_bpermute_b32 v20, v225, v4
	ds_bpermute_b32 v21, v225, v5
	ds_bpermute_b32 v22, v225, v6
	ds_bpermute_b32 v23, v225, v7
	s_waitcnt lgkmcnt(5)
	v_cndmask_b32_e64 v34, v18, v2, s[0:1]
	s_waitcnt lgkmcnt(4)
	v_cndmask_b32_e64 v3, v19, v3, s[0:1]
	s_waitcnt lgkmcnt(3)
	v_cndmask_b32_e64 v4, v20, v4, s[0:1]
	s_waitcnt lgkmcnt(2)
	v_cndmask_b32_e64 v5, v21, v5, s[0:1]
	v_cndmask_b32_e64 v2, v2, v18, s[0:1]
	v_add_f32_e32 v21, s12, v34
	v_add_f32_e32 v3, s13, v3
	v_add_f32_e32 v4, s14, v4
	v_add_f32_e32 v5, s15, v5
	ds_bpermute_b32 v24, v225, v8
	ds_bpermute_b32 v25, v225, v9
	ds_bpermute_b32 v26, v225, v10
	ds_bpermute_b32 v27, v225, v11
	ds_bpermute_b32 v28, v225, v12
	ds_bpermute_b32 v29, v225, v13
	s_waitcnt lgkmcnt(7)
	v_cndmask_b32_e64 v18, v22, v6, s[0:1]
	s_waitcnt lgkmcnt(6)
	v_cndmask_b32_e64 v7, v23, v7, s[0:1]
	v_cndmask_b32_e64 v6, v6, v22, s[0:1]
	v_add_f32_e32 v2, s16, v2
	v_max_f32_e32 v22, v21, v3
	v_max_f32_e32 v23, v4, v5
	v_max3_f32 v22, v22, v23, v2
	ds_bpermute_b32 v30, v225, v14
	ds_bpermute_b32 v31, v225, v15
	ds_bpermute_b32 v32, v225, v16
	ds_bpermute_b32 v33, v225, v17
	v_sub_f32_e32 v21, v21, v22
	v_sub_f32_e32 v3, v3, v22
	v_mul_f32_e32 v21, 0x3fb8aa3b, v21
	v_sub_f32_e32 v4, v4, v22
	v_mul_f32_e32 v3, 0x3fb8aa3b, v3
	v_exp_f32_e32 v21, v21
	s_waitcnt lgkmcnt(9)
	v_cndmask_b32_e64 v8, v24, v8, s[0:1]
	s_waitcnt lgkmcnt(8)
	v_cndmask_b32_e64 v9, v25, v9, s[0:1]
	s_waitcnt lgkmcnt(7)
	v_cndmask_b32_e64 v19, v26, v10, s[0:1]
	s_waitcnt lgkmcnt(6)
	v_cndmask_b32_e64 v11, v27, v11, s[0:1]
	s_waitcnt lgkmcnt(5)
	v_cndmask_b32_e64 v12, v28, v12, s[0:1]
	s_waitcnt lgkmcnt(4)
	v_cndmask_b32_e64 v13, v29, v13, s[0:1]
	v_sub_f32_e32 v5, v5, v22
	v_mul_f32_e32 v4, 0x3fb8aa3b, v4
	v_exp_f32_e32 v3, v3
	v_cndmask_b32_e64 v10, v10, v26, s[0:1]
	v_add_f32_e32 v18, s17, v18
	v_add_f32_e32 v7, s18, v7
	v_add_f32_e32 v8, s19, v8
	v_add_f32_e32 v9, s20, v9
	v_add_f32_e32 v19, s22, v19
	v_add_f32_e32 v11, s23, v11
	v_add_f32_e32 v12, s24, v12
	v_add_f32_e32 v13, s25, v13
	v_sub_f32_e32 v2, v2, v22
	v_mul_f32_e32 v5, 0x3fb8aa3b, v5
	v_exp_f32_e32 v4, v4
	s_waitcnt lgkmcnt(3)
	v_cndmask_b32_e64 v20, v30, v14, s[0:1]
	s_waitcnt lgkmcnt(2)
	v_cndmask_b32_e64 v15, v31, v15, s[0:1]
	s_waitcnt lgkmcnt(1)
	v_cndmask_b32_e64 v16, v32, v16, s[0:1]
	s_waitcnt lgkmcnt(0)
	v_cndmask_b32_e64 v17, v33, v17, s[0:1]
	v_add_f32_e32 v6, s21, v6
	v_add_f32_e32 v10, s26, v10
	v_max_f32_e32 v24, v18, v7
	v_max_f32_e32 v25, v8, v9
	v_max_f32_e32 v26, v19, v11
	v_max_f32_e32 v27, v12, v13
	v_mul_f32_e32 v2, 0x3fb8aa3b, v2
	v_exp_f32_e32 v5, v5
	v_cndmask_b32_e64 v14, v14, v30, s[0:1]
	v_add_f32_e32 v20, s27, v20
	v_add_f32_e32 v15, s28, v15
	v_add_f32_e32 v16, s29, v16
	v_add_f32_e32 v17, s30, v17
	v_max3_f32 v23, v24, v25, v6
	v_max3_f32 v24, v26, v27, v10
	v_exp_f32_e32 v2, v2
	v_add_f32_e32 v22, 0, v21
	v_add_f32_e32 v14, s31, v14
	v_max_f32_e32 v28, v20, v15
	v_max_f32_e32 v29, v16, v17
	v_sub_f32_e32 v19, v19, v24
	v_add_f32_e32 v22, v3, v22
	v_max3_f32 v25, v28, v29, v14
	v_sub_f32_e32 v11, v11, v24
	v_mul_f32_e32 v19, 0x3fb8aa3b, v19
	v_add_f32_e32 v22, v4, v22
	v_sub_f32_e32 v18, v18, v23
	v_sub_f32_e32 v12, v12, v24
	v_sub_f32_e32 v20, v20, v25
	v_mul_f32_e32 v11, 0x3fb8aa3b, v11
	v_exp_f32_e32 v19, v19
	v_add_f32_e32 v22, v5, v22
	v_sub_f32_e32 v7, v7, v23
	v_sub_f32_e32 v13, v13, v24
	v_mul_f32_e32 v18, 0x3fb8aa3b, v18
	v_mul_f32_e32 v12, 0x3fb8aa3b, v12
	v_mul_f32_e32 v20, 0x3fb8aa3b, v20
	v_exp_f32_e32 v11, v11
	v_add_f32_e32 v22, v2, v22
	v_sub_f32_e32 v15, v15, v25
	v_sub_f32_e32 v8, v8, v23
	v_sub_f32_e32 v10, v10, v24
	v_mul_f32_e32 v7, 0x3fb8aa3b, v7
	v_mul_f32_e32 v13, 0x3fb8aa3b, v13
	v_exp_f32_e32 v18, v18
	v_exp_f32_e32 v12, v12
	v_exp_f32_e32 v20, v20
	v_rcp_f32_e32 v22, v22
	v_mul_f32_e32 v15, 0x3fb8aa3b, v15
	v_sub_f32_e32 v16, v16, v25
	v_sub_f32_e32 v9, v9, v23
	v_mul_f32_e32 v8, 0x3fb8aa3b, v8
	v_mul_f32_e32 v10, 0x3fb8aa3b, v10
	v_exp_f32_e32 v7, v7
	v_exp_f32_e32 v13, v13
	v_exp_f32_e32 v15, v15
	v_mul_f32_e32 v16, 0x3fb8aa3b, v16
	v_sub_f32_e32 v17, v17, v25
	v_sub_f32_e32 v6, v6, v23
	v_mul_f32_e32 v9, 0x3fb8aa3b, v9
	v_exp_f32_e32 v8, v8
	v_exp_f32_e32 v10, v10
	v_add_f32_e32 v24, 0, v19
	v_exp_f32_e32 v16, v16
	v_mul_f32_e32 v17, 0x3fb8aa3b, v17
	v_sub_f32_e32 v14, v14, v25
	v_mul_f32_e32 v6, 0x3fb8aa3b, v6
	v_exp_f32_e32 v9, v9
	v_add_f32_e32 v24, v11, v24
	v_exp_f32_e32 v17, v17
	v_mul_f32_e32 v14, 0x3fb8aa3b, v14
	v_exp_f32_e32 v6, v6
	v_add_f32_e32 v23, 0, v18
	v_add_f32_e32 v24, v12, v24
	v_mul_f32_e32 v21, v21, v22
	v_mul_f32_e32 v3, v3, v22
	v_mul_f32_e32 v4, v4, v22
	v_mul_f32_e32 v5, v5, v22
	v_mul_f32_e32 v2, v2, v22
	v_add_f32_e32 v22, 0, v20
	v_exp_f32_e32 v14, v14
	v_add_f32_e32 v23, v7, v23
	v_add_f32_e32 v24, v13, v24
	v_add_f32_e32 v22, v15, v22
	v_add_f32_e32 v23, v8, v23
	v_add_f32_e32 v24, v10, v24
	v_add_f32_e32 v22, v16, v22
	v_add_f32_e32 v23, v9, v23
	v_rcp_f32_e32 v24, v24
	v_add_f32_e32 v22, v17, v22
	v_add_f32_e32 v23, v6, v23
	v_add_f32_e32 v22, v14, v22
	v_rcp_f32_e32 v23, v23
	v_rcp_f32_e32 v22, v22
	v_mul_f32_e32 v19, v19, v24
	v_mul_f32_e32 v11, v11, v24
	v_mul_f32_e32 v12, v12, v24
	v_mul_f32_e32 v13, v13, v24
	v_cndmask_b32_e64 v19, v19, v21, s[4:5]
	v_cndmask_b32_e64 v3, v11, v3, s[4:5]
	v_mul_f32_e32 v18, v18, v23
	v_mul_f32_e32 v10, v10, v24
	v_mul_f32_e32 v20, v20, v22
	ds_write2st64_b32 v222, v19, v3 offset1:8
	v_cndmask_b32_e64 v3, v12, v4, s[4:5]
	v_cndmask_b32_e64 v4, v13, v5, s[4:5]
	v_mul_f32_e32 v7, v7, v23
	v_mul_f32_e32 v8, v8, v23
	v_mul_f32_e32 v15, v15, v22
	v_mul_f32_e32 v16, v16, v22
	ds_write2st64_b32 v222, v3, v4 offset0:16 offset1:24
	v_cndmask_b32_e64 v2, v10, v2, s[4:5]
	v_cndmask_b32_e64 v3, v20, v18, s[4:5]
	v_mul_f32_e32 v9, v9, v23
	v_mul_f32_e32 v6, v6, v23
	v_mul_f32_e32 v17, v17, v22
	v_mul_f32_e32 v14, v14, v22
	ds_write2st64_b32 v222, v2, v3 offset0:32 offset1:40
	v_cndmask_b32_e64 v2, v15, v7, s[4:5]
	v_cndmask_b32_e64 v3, v16, v8, s[4:5]
	ds_write2st64_b32 v222, v2, v3 offset0:48 offset1:56
	v_cndmask_b32_e64 v2, v17, v9, s[4:5]
	v_cndmask_b32_e64 v3, v14, v6, s[4:5]
	s_movk_i32 s13, 0x200
	s_movk_i32 s26, 0x3844
	s_movk_i32 s27, 0x2bdb
	s_mov_b32 s28, 0xb160
	s_movk_i32 s29, 0x34e2
	s_mov_b32 s30, 0xad10
	s_mov_b32 s31, 0xb1ec
	s_brev_b32 s12, 60
	s_mov_b64 s[14:15], s[44:45]
	ds_write2st64_b32 v222, v2, v3 offset0:64 offset1:72
	v_readfirstlane_b32 s53, v0
	s_lshl_b32 s53, s53, 4
	s_and_b32 s54, s53, 0xfffff000
	s_and_b32 s53, s53, 0xfffffc00
	s_add_i32 s53, s53, 0x8000
	s_sub_i32 s54, 0x8000, s54
	s_branch .LBB1_26

.LBB1_25:
	s_add_i32 s16, s33, 1
	s_cmp_lg_u32 s33, 2
	s_cselect_b32 s33, s16, 0
	s_add_i32 s40, s40, 1
	s_add_u32 s14, s14, 0x9000
	s_addc_u32 s15, s15, 0
	s_cmp_eq_u32 s40, 40
	s_waitcnt vmcnt(5) lgkmcnt(0)
	s_barrier
	s_cbranch_scc1 .LBB1_82

.LBB1_35:
	v_add_u32_e32 v82, s18, v247
	ds_read_b128 v[66:69], v231 offset:32768
	ds_read_b128 v[70:73], v231 offset:32800
	ds_read_b128 v[74:77], v231 offset:32832
	ds_read_b128 v[78:81], v231 offset:32864
	ds_read_b128 v[190:193], v82 offset:32768
	ds_read_b128 v[194:197], v82 offset:33792
	ds_read_b128 v[198:201], v82 offset:34816
	ds_read_b128 v[202:205], v82 offset:35840
	ds_read_b128 v[212:215], v82 offset:36864
	ds_read_b128 v[232:235], v82 offset:37888
	ds_read_b128 v[236:239], v82 offset:38912
	ds_read_b128 v[240:243], v82 offset:39936
	s_waitcnt lgkmcnt(7)
	v_mfma_f32_32x32x16_f16 v[66:81], v[190:193], v[146:149], v[66:81]
	s_add_i32 s17, s18, 0xffff7000
	s_cmp_lg_u32 s33, 0
	s_cselect_b32 s17, s17, 0x12000
	s_waitcnt lgkmcnt(6)
	v_mfma_f32_32x32x16_f16 v[66:81], v[194:197], v[150:153], v[66:81]
	s_waitcnt lgkmcnt(5)
	v_mfma_f32_32x32x16_f16 v[66:81], v[198:201], v[154:157], v[66:81]
	s_waitcnt lgkmcnt(4)
	v_mfma_f32_32x32x16_f16 v[66:81], v[202:205], v[158:161], v[66:81]
	s_add_i32 s17, s17, s53
	s_add_i32 m0, s17, 0
	s_add_u32 s18, s14, 0x372000
	s_addc_u32 s19, s15, 0
	global_load_lds_dwordx4 v226, s[18:19]
	s_waitcnt lgkmcnt(3)
	v_mfma_f32_32x32x16_f16 v[66:81], v[212:215], v[162:165], v[66:81]
	s_add_i32 m0, s17, 0x2000
	s_add_u32 s18, s14, 0x374000
	s_addc_u32 s19, s15, 0
	global_load_lds_dwordx4 v226, s[18:19]
	s_waitcnt lgkmcnt(2)
	v_mfma_f32_32x32x16_f16 v[66:81], v[232:235], v[166:169], v[66:81]
	s_add_i32 m0, s17, 0x4000
	s_add_u32 s18, s14, 0x376000
	s_addc_u32 s19, s15, 0
	global_load_lds_dwordx4 v226, s[18:19]
	s_waitcnt lgkmcnt(1)
	v_mfma_f32_32x32x16_f16 v[66:81], v[236:239], v[170:173], v[66:81]
	s_add_i32 m0, s17, 0x6000
	s_add_u32 s18, s14, 0x378000
	s_addc_u32 s19, s15, 0
	global_load_lds_dwordx4 v226, s[18:19]
	s_waitcnt lgkmcnt(0)
	v_mfma_f32_32x32x16_f16 v[66:81], v[240:243], v[174:177], v[66:81]
	s_add_i32 m0, s17, s54
	s_add_u32 s18, s14, 0x37a000
	s_addc_u32 s19, s15, 0
	global_load_lds_dwordx4 v224, s[18:19]
	ds_read_b128 v[190:193], v82 offset:40960
	ds_read_b128 v[194:197], v82 offset:41984
	ds_read_b128 v[198:201], v82 offset:43008
	ds_read_b128 v[202:205], v82 offset:44032
	ds_read_b128 v[212:215], v82 offset:45056
	ds_read_b128 v[232:235], v82 offset:46080
	ds_read_b128 v[236:239], v82 offset:47104
	ds_read_b128 v[240:243], v82 offset:48128
	v_cvt_pk_f16_f32 v66, v66, v67
	v_cvt_pk_f16_f32 v67, v68, v69
	v_cvt_pk_f16_f32 v68, v70, v71
	v_cvt_pk_f16_f32 v69, v72, v73
	v_and_b32_e32 v70, 0x7fff7fff, v66
	v_and_b32_e32 v71, 0x7fff7fff, v67
	v_and_b32_e32 v72, 0x7fff7fff, v68
	v_and_b32_e32 v73, 0x7fff7fff, v69
	v_pk_min_f16 v70, v70, v229
	v_pk_min_f16 v71, v71, v229
	v_pk_min_f16 v72, v72, v229
	v_pk_min_f16 v73, v73, v229
	v_pk_max_f16 v66, v66, v228
	v_pk_max_f16 v67, v67, v228
	s_nop 0
	v_pk_fma_f16 v70, v70, s26, -1.0 op_sel_hi:[1,0,0]
	v_pk_fma_f16 v71, v71, s26, -1.0 op_sel_hi:[1,0,0]
	v_pk_fma_f16 v72, v72, s26, -1.0 op_sel_hi:[1,0,0]
	v_pk_fma_f16 v73, v73, s26, -1.0 op_sel_hi:[1,0,0]
	v_pk_fma_f16 v82, v70, s27, v230 op_sel_hi:[1,0,0]
	v_pk_fma_f16 v83, v71, s27, v230 op_sel_hi:[1,0,0]
	v_pk_fma_f16 v144, v72, s27, v230 op_sel_hi:[1,0,0]
	v_pk_fma_f16 v145, v73, s27, v230 op_sel_hi:[1,0,0]
	v_pk_fma_f16 v82, v70, v82, s28 op_sel_hi:[1,1,0]
	v_pk_fma_f16 v83, v71, v83, s28 op_sel_hi:[1,1,0]
	v_pk_fma_f16 v144, v72, v144, s28 op_sel_hi:[1,1,0]
	v_pk_fma_f16 v145, v73, v145, s28 op_sel_hi:[1,1,0]
	v_pk_fma_f16 v82, v70, v82, s29 op_sel_hi:[1,1,0]
	v_pk_fma_f16 v83, v71, v83, s29 op_sel_hi:[1,1,0]
	v_pk_fma_f16 v144, v72, v144, s29 op_sel_hi:[1,1,0]
	v_pk_fma_f16 v145, v73, v145, s29 op_sel_hi:[1,1,0]
	v_pk_fma_f16 v82, v70, v82, s30 op_sel_hi:[1,1,0]
	v_pk_fma_f16 v83, v71, v83, s30 op_sel_hi:[1,1,0]
	v_pk_fma_f16 v144, v72, v144, s30 op_sel_hi:[1,1,0]
	v_pk_fma_f16 v145, v73, v145, s30 op_sel_hi:[1,1,0]
	v_pk_fma_f16 v82, v70, v82, s31 op_sel_hi:[1,1,0]
	v_pk_fma_f16 v83, v71, v83, s31 op_sel_hi:[1,1,0]
	v_pk_fma_f16 v144, v72, v144, s31 op_sel_hi:[1,1,0]
	v_pk_fma_f16 v145, v73, v145, s31 op_sel_hi:[1,1,0]
	v_pk_fma_f16 v82, v70, v82, s41 op_sel_hi:[1,1,0]
	v_pk_fma_f16 v83, v71, v83, s41 op_sel_hi:[1,1,0]
	v_pk_fma_f16 v144, v72, v144, s41 op_sel_hi:[1,1,0]
	v_pk_fma_f16 v145, v73, v145, s41 op_sel_hi:[1,1,0]
	v_pk_max_f16 v68, v68, v228
	v_pk_max_f16 v69, v69, v228
	v_pk_fma_f16 v70, v70, v82, s42 op_sel_hi:[1,1,0]
	v_pk_fma_f16 v71, v71, v83, s42 op_sel_hi:[1,1,0]
	v_pk_fma_f16 v72, v72, v144, s42 op_sel_hi:[1,1,0]
	v_pk_fma_f16 v73, v73, v145, s42 op_sel_hi:[1,1,0]
	v_pk_add_f16 v66, v66, v70
	v_pk_add_f16 v67, v67, v71
	v_pk_add_f16 v68, v68, v72
	v_pk_add_f16 v69, v69, v73
	v_cvt_pk_f16_f32 v70, v74, v75
	v_cvt_pk_f16_f32 v71, v76, v77
	v_cvt_pk_f16_f32 v72, v78, v79
	v_cvt_pk_f16_f32 v73, v80, v81
	v_and_b32_e32 v74, 0x7fff7fff, v70
	v_and_b32_e32 v75, 0x7fff7fff, v71
	v_and_b32_e32 v76, 0x7fff7fff, v72
	v_and_b32_e32 v77, 0x7fff7fff, v73
	v_pk_min_f16 v74, v74, v229
	v_pk_min_f16 v75, v75, v229
	v_pk_min_f16 v76, v76, v229
	v_pk_min_f16 v77, v77, v229
	s_waitcnt lgkmcnt(7)
	v_mfma_f32_32x32x16_f16 v[2:17], v[190:193], v[66:69], v[2:17]
	v_pk_fma_f16 v74, v74, s26, -1.0 op_sel_hi:[1,0,0]
	v_pk_fma_f16 v75, v75, s26, -1.0 op_sel_hi:[1,0,0]
	v_pk_fma_f16 v76, v76, s26, -1.0 op_sel_hi:[1,0,0]
	v_pk_fma_f16 v77, v77, s26, -1.0 op_sel_hi:[1,0,0]
	v_pk_fma_f16 v78, v74, s27, v230 op_sel_hi:[1,0,0]
	v_pk_fma_f16 v79, v75, s27, v230 op_sel_hi:[1,0,0]
	v_pk_fma_f16 v80, v76, s27, v230 op_sel_hi:[1,0,0]
	v_pk_fma_f16 v81, v77, s27, v230 op_sel_hi:[1,0,0]
	s_waitcnt lgkmcnt(5)
	v_mfma_f32_32x32x16_f16 v[18:33], v[198:201], v[66:69], v[18:33]
	v_pk_fma_f16 v78, v74, v78, s28 op_sel_hi:[1,1,0]
	v_pk_fma_f16 v79, v75, v79, s28 op_sel_hi:[1,1,0]
	v_pk_fma_f16 v80, v76, v80, s28 op_sel_hi:[1,1,0]
	v_pk_fma_f16 v81, v77, v81, s28 op_sel_hi:[1,1,0]
	v_pk_fma_f16 v78, v74, v78, s29 op_sel_hi:[1,1,0]
	v_pk_fma_f16 v79, v75, v79, s29 op_sel_hi:[1,1,0]
	v_pk_fma_f16 v80, v76, v80, s29 op_sel_hi:[1,1,0]
	s_waitcnt lgkmcnt(3)
	v_mfma_f32_32x32x16_f16 v[34:49], v[212:215], v[66:69], v[34:49]
	v_pk_fma_f16 v81, v77, v81, s29 op_sel_hi:[1,1,0]
	v_pk_fma_f16 v78, v74, v78, s30 op_sel_hi:[1,1,0]
	v_pk_fma_f16 v79, v75, v79, s30 op_sel_hi:[1,1,0]
	v_pk_fma_f16 v80, v76, v80, s30 op_sel_hi:[1,1,0]
	v_pk_fma_f16 v81, v77, v81, s30 op_sel_hi:[1,1,0]
	v_pk_fma_f16 v78, v74, v78, s31 op_sel_hi:[1,1,0]
	v_pk_fma_f16 v79, v75, v79, s31 op_sel_hi:[1,1,0]
	s_waitcnt lgkmcnt(1)
	v_mfma_f32_32x32x16_f16 v[50:65], v[236:239], v[66:69], v[50:65]
	v_pk_fma_f16 v80, v76, v80, s31 op_sel_hi:[1,1,0]
	v_pk_fma_f16 v81, v77, v81, s31 op_sel_hi:[1,1,0]
	v_pk_fma_f16 v78, v74, v78, s41 op_sel_hi:[1,1,0]
	v_pk_fma_f16 v79, v75, v79, s41 op_sel_hi:[1,1,0]
	v_pk_fma_f16 v80, v76, v80, s41 op_sel_hi:[1,1,0]
	v_pk_fma_f16 v81, v77, v81, s41 op_sel_hi:[1,1,0]
	v_pk_max_f16 v70, v70, v228
	v_pk_max_f16 v71, v71, v228
	v_pk_max_f16 v72, v72, v228
	v_pk_max_f16 v73, v73, v228
	v_pk_fma_f16 v74, v74, v78, s42 op_sel_hi:[1,1,0]
	v_pk_fma_f16 v75, v75, v79, s42 op_sel_hi:[1,1,0]
	v_pk_fma_f16 v76, v76, v80, s42 op_sel_hi:[1,1,0]
	v_pk_fma_f16 v77, v77, v81, s42 op_sel_hi:[1,1,0]
	v_pk_add_f16 v70, v70, v74
	v_pk_add_f16 v71, v71, v75
	v_pk_add_f16 v72, v72, v76
	v_pk_add_f16 v73, v73, v77
	s_cmp_lg_u32 s16, 7
	s_nop 0
	v_mfma_f32_32x32x16_f16 v[2:17], v[194:197], v[70:73], v[2:17]
	v_mfma_f32_32x32x16_f16 v[18:33], v[202:205], v[70:73], v[18:33]
	v_mfma_f32_32x32x16_f16 v[34:49], v[232:235], v[70:73], v[34:49]
	s_waitcnt lgkmcnt(0)
	v_mfma_f32_32x32x16_f16 v[50:65], v[240:243], v[70:73], v[50:65]
	s_cbranch_scc1 .LBB1_25
	ds_read_b128 v[198:201], v231 offset:33280
	ds_read_b128 v[190:193], v231 offset:33312
	ds_read_b128 v[202:205], v231 offset:33792
	ds_read_b128 v[194:197], v231 offset:33824
	ds_read_b128 v[74:77], v231 offset:33344
	ds_read_b128 v[66:69], v231 offset:33376
	ds_read_b128 v[78:81], v231 offset:33856
	ds_read_b128 v[70:73], v231 offset:33888
	s_lshr_b32 s24, s40, 3
	s_cmp_lt_u32 s40, 16
	s_cselect_b64 s[16:17], -1, 0
	s_cmp_gt_u32 s40, 15
	s_cselect_b64 s[22:23], -1, 0
	s_and_saveexec_b64 s[18:19], s[8:9]
	s_xor_b64 s[18:19], exec, s[18:19]
	s_cbranch_execz .LBB1_41
	s_mov_b64 s[20:21], -1
	s_and_b64 vcc, exec, s[22:23]
	s_cbranch_vccz .LBB1_39
	s_cmp_eq_u32 s24, 2
	s_cselect_b32 s25, 2, -1
	s_mov_b64 s[20:21], 0
